# speedup vs baseline: 1.0887x; 1.0028x over previous
_Z6k_poolPKDF16_PKiS2_PKfS4_S4_Pf:
	s_load_dwordx8 s[4:11], s[0:1], 0x0
	s_load_dwordx4 s[20:23], s[0:1], 0x28
	v_mov_b32_e32 v61, 0
	s_ashr_i32 s3, s2, 31
	s_lshl_b64 s[12:13], s[2:3], 2
	v_lshrrev_b32_e32 v37, 4, v0
	v_bfe_u32 v1, v0, 3, 1
	s_waitcnt lgkmcnt(0)
	s_mov_b64 s[16:17], s[4:5]
	s_add_u32 s6, s6, s12
	s_addc_u32 s7, s7, s13
	s_lshl_b32 s12, s2, 9
	s_ashr_i32 s13, s12, 31
	s_lshl_b64 s[12:13], s[12:13], 2
	s_add_u32 s8, s8, s12
	v_add_u32_e32 v1, v1, v37
	s_addc_u32 s9, s9, s13
	v_lshlrev_b32_e32 v3, 2, v1
	global_load_dword v2, v3, s[8:9]
	global_load_dword v4, v3, s[8:9] offset:256
	global_load_dword v10, v3, s[8:9] offset:512
	global_load_dword v14, v3, s[8:9] offset:768
	global_load_dword v18, v3, s[8:9] offset:1024
	global_load_dword v24, v3, s[8:9] offset:1280
	v_min_u32_e32 v1, 63, v1
	v_lshlrev_b32_e32 v1, 2, v1
	global_load_dword v6, v3, s[8:9] offset:1536
	global_load_dword v8, v1, s[8:9] offset:1792
	v_and_b32_e32 v36, 15, v0
	v_mov_b32_e32 v13, 0
	v_lshlrev_b32_e32 v12, 4, v36
	v_lshlrev_b32_e32 v51, 4, v36
	v_lshl_add_u64 v[22:23], s[4:5], 0, v[12:13]
	v_mbcnt_lo_u32_b32 v1, -1, 0
	s_load_dwordx2 s[4:5], s[0:1], 0x20
	v_mbcnt_hi_u32_b32 v1, -1, v1
	v_and_b32_e32 v38, 63, v0
	v_and_b32_e32 v9, 56, v1
	v_lshlrev_b32_e32 v7, 2, v38
	v_cmp_eq_u32_e32 vcc, 56, v9
	s_load_dword s6, s[6:7], 0x0
	v_mov_b32_e32 v40, 0xfc00fc00
	v_cndmask_b32_e64 v9, 8, 0, vcc
	v_add_lshl_u32 v49, v9, v1, 2
	v_or_b32_e32 v41, 64, v37
	v_or_b32_e32 v46, 0x80, v37
	s_mov_b32 s3, 0xfc00
	v_or_b32_e32 v47, 0xc0, v37
	v_or_b32_e32 v48, 0x100, v37
	s_waitcnt vmcnt(7)
	v_lshl_add_u32 v3, v2, 8, v51
	s_waitcnt vmcnt(6)
	global_load_dwordx4 v[30:33], v3, s[16:17]
	v_lshl_add_u32 v3, v4, 8, v51
	s_waitcnt vmcnt(6)
	global_load_dwordx4 v[26:29], v3, s[16:17]
	v_lshl_add_u32 v3, v10, 8, v51
	s_waitcnt vmcnt(6)
	global_load_dwordx4 v[10:13], v3, s[16:17]
	v_lshl_add_u32 v3, v14, 8, v51
	s_waitcnt vmcnt(6)
	global_load_dwordx4 v[14:17], v3, s[16:17]
	v_lshl_add_u32 v3, v18, 8, v51
	s_waitcnt vmcnt(6)
	global_load_dwordx4 v[18:21], v3, s[16:17]
	v_lshl_add_u32 v3, v24, 8, v51
	global_load_dwordx4 v[2:5], v3, s[16:17]
	s_nop 0
	global_load_dword v39, v7, s[10:11]
	s_waitcnt lgkmcnt(0)
	global_load_dword v34, v7, s[4:5]
	global_load_dword v35, v7, s[4:5] offset:256
	s_waitcnt vmcnt(10)
	v_lshl_add_u32 v42, v6, 8, v51
	s_waitcnt vmcnt(9)
	v_lshl_add_u32 v44, v8, 8, v51
	global_load_dwordx4 v[22:25], v42, s[16:17]
	global_load_dwordx4 v[6:9], v44, s[16:17]
	global_load_dwordx2 v[62:63], v61, s[20:21]
	s_min_i32 s4, s6, 0x1ff
	s_waitcnt vmcnt(11)
	v_cmp_gt_i32_e32 vcc, s4, v37
	v_mov_b32_dpp v54, v30 row_shl:8 row_mask:0xf bank_mask:0xf bound_ctrl:0
	v_mov_b32_dpp v55, v31 row_shl:8 row_mask:0xf bank_mask:0xf bound_ctrl:0
	v_mov_b32_dpp v56, v32 row_shl:8 row_mask:0xf bank_mask:0xf bound_ctrl:0
	v_mov_b32_dpp v57, v33 row_shl:8 row_mask:0xf bank_mask:0xf bound_ctrl:0
	v_pk_add_f16 v30, v30, v54
	v_pk_add_f16 v31, v31, v55
	v_pk_add_f16 v32, v32, v56
	v_pk_add_f16 v33, v33, v57
	v_cndmask_b32_e32 v30, v40, v30, vcc
	v_cndmask_b32_e32 v31, v40, v31, vcc
	v_cndmask_b32_e32 v32, v40, v32, vcc
	v_cndmask_b32_e32 v33, v40, v33, vcc
	s_waitcnt vmcnt(10)
	v_cmp_gt_i32_e32 vcc, s4, v41
	v_mov_b32_dpp v54, v26 row_shl:8 row_mask:0xf bank_mask:0xf bound_ctrl:0
	v_mov_b32_dpp v55, v27 row_shl:8 row_mask:0xf bank_mask:0xf bound_ctrl:0
	v_mov_b32_dpp v56, v28 row_shl:8 row_mask:0xf bank_mask:0xf bound_ctrl:0
	v_mov_b32_dpp v57, v29 row_shl:8 row_mask:0xf bank_mask:0xf bound_ctrl:0
	v_pk_add_f16 v26, v26, v54
	v_pk_add_f16 v27, v27, v55
	v_pk_add_f16 v28, v28, v56
	v_pk_add_f16 v29, v29, v57
	v_cndmask_b32_e32 v26, v40, v26, vcc
	v_cndmask_b32_e32 v27, v40, v27, vcc
	v_cndmask_b32_e32 v28, v40, v28, vcc
	v_cndmask_b32_e32 v29, v40, v29, vcc
	v_pk_max_f16 v30, v30, v26
	v_pk_max_f16 v31, v31, v27
	v_pk_max_f16 v32, v32, v28
	v_pk_max_f16 v33, v33, v29
	s_waitcnt vmcnt(9)
	v_cmp_gt_i32_e32 vcc, s4, v46
	v_mov_b32_dpp v54, v10 row_shl:8 row_mask:0xf bank_mask:0xf bound_ctrl:0
	v_mov_b32_dpp v55, v11 row_shl:8 row_mask:0xf bank_mask:0xf bound_ctrl:0
	v_mov_b32_dpp v56, v12 row_shl:8 row_mask:0xf bank_mask:0xf bound_ctrl:0
	v_mov_b32_dpp v57, v13 row_shl:8 row_mask:0xf bank_mask:0xf bound_ctrl:0
	v_pk_add_f16 v10, v10, v54
	v_pk_add_f16 v11, v11, v55
	v_pk_add_f16 v12, v12, v56
	v_pk_add_f16 v13, v13, v57
	v_cndmask_b32_e32 v10, v40, v10, vcc
	v_cndmask_b32_e32 v11, v40, v11, vcc
	v_cndmask_b32_e32 v12, v40, v12, vcc
	v_cndmask_b32_e32 v13, v40, v13, vcc
	v_pk_max_f16 v30, v30, v10
	v_pk_max_f16 v31, v31, v11
	v_pk_max_f16 v32, v32, v12
	v_pk_max_f16 v33, v33, v13
	s_waitcnt vmcnt(8)
	v_cmp_gt_i32_e32 vcc, s4, v47
	v_mov_b32_dpp v54, v14 row_shl:8 row_mask:0xf bank_mask:0xf bound_ctrl:0
	v_mov_b32_dpp v55, v15 row_shl:8 row_mask:0xf bank_mask:0xf bound_ctrl:0
	v_mov_b32_dpp v56, v16 row_shl:8 row_mask:0xf bank_mask:0xf bound_ctrl:0
	v_mov_b32_dpp v57, v17 row_shl:8 row_mask:0xf bank_mask:0xf bound_ctrl:0
	v_pk_add_f16 v14, v14, v54
	v_pk_add_f16 v15, v15, v55
	v_pk_add_f16 v16, v16, v56
	v_pk_add_f16 v17, v17, v57
	v_cndmask_b32_e32 v14, v40, v14, vcc
	v_cndmask_b32_e32 v15, v40, v15, vcc
	v_cndmask_b32_e32 v16, v40, v16, vcc
	v_cndmask_b32_e32 v17, v40, v17, vcc
	v_pk_max_f16 v30, v30, v14
	v_pk_max_f16 v31, v31, v15
	v_pk_max_f16 v32, v32, v16
	v_pk_max_f16 v33, v33, v17
	s_waitcnt vmcnt(7)
	v_cmp_gt_i32_e32 vcc, s4, v48
	v_mov_b32_dpp v54, v18 row_shl:8 row_mask:0xf bank_mask:0xf bound_ctrl:0
	v_mov_b32_dpp v55, v19 row_shl:8 row_mask:0xf bank_mask:0xf bound_ctrl:0
	v_mov_b32_dpp v56, v20 row_shl:8 row_mask:0xf bank_mask:0xf bound_ctrl:0
	v_mov_b32_dpp v57, v21 row_shl:8 row_mask:0xf bank_mask:0xf bound_ctrl:0
	v_pk_add_f16 v18, v18, v54
	v_pk_add_f16 v19, v19, v55
	v_pk_add_f16 v20, v20, v56
	v_pk_add_f16 v21, v21, v57
	v_cndmask_b32_e32 v18, v40, v18, vcc
	v_cndmask_b32_e32 v19, v40, v19, vcc
	v_cndmask_b32_e32 v20, v40, v20, vcc
	v_cndmask_b32_e32 v21, v40, v21, vcc
	v_pk_max_f16 v30, v30, v18
	v_pk_max_f16 v31, v31, v19
	v_pk_max_f16 v32, v32, v20
	v_pk_max_f16 v33, v33, v21
	v_or_b32_e32 v52, 0x140, v37
	s_waitcnt vmcnt(6)
	v_cmp_gt_i32_e32 vcc, s4, v52
	v_mov_b32_dpp v54, v2 row_shl:8 row_mask:0xf bank_mask:0xf bound_ctrl:0
	v_mov_b32_dpp v55, v3 row_shl:8 row_mask:0xf bank_mask:0xf bound_ctrl:0
	v_mov_b32_dpp v56, v4 row_shl:8 row_mask:0xf bank_mask:0xf bound_ctrl:0
	v_mov_b32_dpp v57, v5 row_shl:8 row_mask:0xf bank_mask:0xf bound_ctrl:0
	v_pk_add_f16 v2, v2, v54
	v_pk_add_f16 v3, v3, v55
	v_pk_add_f16 v4, v4, v56
	v_pk_add_f16 v5, v5, v57
	v_cndmask_b32_e32 v2, v40, v2, vcc
	v_cndmask_b32_e32 v3, v40, v3, vcc
	v_cndmask_b32_e32 v4, v40, v4, vcc
	v_cndmask_b32_e32 v5, v40, v5, vcc
	v_pk_max_f16 v30, v30, v2
	v_pk_max_f16 v31, v31, v3
	v_pk_max_f16 v32, v32, v4
	v_pk_max_f16 v33, v33, v5
	v_or_b32_e32 v52, 0x180, v37
	s_waitcnt vmcnt(2)
	v_cmp_gt_i32_e32 vcc, s4, v52
	v_mov_b32_dpp v54, v22 row_shl:8 row_mask:0xf bank_mask:0xf bound_ctrl:0
	v_mov_b32_dpp v55, v23 row_shl:8 row_mask:0xf bank_mask:0xf bound_ctrl:0
	v_mov_b32_dpp v56, v24 row_shl:8 row_mask:0xf bank_mask:0xf bound_ctrl:0
	v_mov_b32_dpp v57, v25 row_shl:8 row_mask:0xf bank_mask:0xf bound_ctrl:0
	v_pk_add_f16 v22, v22, v54
	v_pk_add_f16 v23, v23, v55
	v_pk_add_f16 v24, v24, v56
	v_pk_add_f16 v25, v25, v57
	v_cndmask_b32_e32 v22, v40, v22, vcc
	v_cndmask_b32_e32 v23, v40, v23, vcc
	v_cndmask_b32_e32 v24, v40, v24, vcc
	v_cndmask_b32_e32 v25, v40, v25, vcc
	v_pk_max_f16 v30, v30, v22
	v_pk_max_f16 v31, v31, v23
	v_pk_max_f16 v32, v32, v24
	v_pk_max_f16 v33, v33, v25
	v_or_b32_e32 v52, 0x1c0, v37
	s_waitcnt vmcnt(1)
	v_cmp_gt_i32_e32 vcc, s4, v52
	v_mov_b32_dpp v54, v6 row_shl:8 row_mask:0xf bank_mask:0xf bound_ctrl:0
	v_mov_b32_dpp v55, v7 row_shl:8 row_mask:0xf bank_mask:0xf bound_ctrl:0
	v_mov_b32_dpp v56, v8 row_shl:8 row_mask:0xf bank_mask:0xf bound_ctrl:0
	v_mov_b32_dpp v57, v9 row_shl:8 row_mask:0xf bank_mask:0xf bound_ctrl:0
	v_pk_add_f16 v6, v6, v54
	v_pk_add_f16 v7, v7, v55
	v_pk_add_f16 v8, v8, v56
	v_pk_add_f16 v9, v9, v57
	v_cndmask_b32_e32 v6, v40, v6, vcc
	v_cndmask_b32_e32 v7, v40, v7, vcc
	v_cndmask_b32_e32 v8, v40, v8, vcc
	v_cndmask_b32_e32 v9, v40, v9, vcc
	v_pk_max_f16 v30, v30, v6
	v_pk_max_f16 v31, v31, v7
	v_pk_max_f16 v32, v32, v8
	v_pk_max_f16 v33, v33, v9
	v_mov_b32_e32 v54, v30
	v_mov_b32_e32 v55, v31
	v_mov_b32_e32 v56, v32
	v_mov_b32_e32 v57, v33
	v_lshlrev_b32_e32 v2, 2, v0
	s_nop 0
	v_permlane32_swap_b32_e32 v30, v54
	v_permlane32_swap_b32_e32 v31, v55
	v_permlane32_swap_b32_e32 v32, v56
	v_permlane32_swap_b32_e32 v33, v57
	v_pk_max_f16 v30, v30, v54
	v_pk_max_f16 v31, v31, v55
	v_pk_max_f16 v32, v32, v56
	v_pk_max_f16 v33, v33, v57
	v_mov_b32_e32 v54, v30
	v_mov_b32_e32 v55, v31
	v_mov_b32_e32 v56, v32
	v_mov_b32_e32 v57, v33
	s_nop 1
	v_permlane16_swap_b32_e32 v30, v54
	v_permlane16_swap_b32_e32 v31, v55
	v_permlane16_swap_b32_e32 v32, v56
	v_permlane16_swap_b32_e32 v33, v57
	v_pk_max_f16 v30, v30, v54
	v_pk_max_f16 v31, v31, v55
	v_pk_max_f16 v32, v32, v56
	v_pk_max_f16 v33, v33, v57
	v_cmp_gt_u32_e32 vcc, 8, v38
	s_and_saveexec_b64 s[4:5], vcc
	s_cbranch_execz .LBB2_2
	v_cvt_f32_f16_e32 v4, v30
	v_cvt_f32_f16_sdwa v5, v30 dst_sel:DWORD dst_unused:UNUSED_PAD src0_sel:WORD_1
	v_cvt_f32_f16_e32 v6, v31
	v_cvt_f32_f16_sdwa v7, v31 dst_sel:DWORD dst_unused:UNUSED_PAD src0_sel:WORD_1
	v_cvt_f32_f16_e32 v8, v32
	v_cvt_f32_f16_sdwa v9, v32 dst_sel:DWORD dst_unused:UNUSED_PAD src0_sel:WORD_1
	v_cvt_f32_f16_e32 v10, v33
	v_cvt_f32_f16_sdwa v11, v33 dst_sel:DWORD dst_unused:UNUSED_PAD src0_sel:WORD_1
	v_and_b32_e32 v3, 0xf00, v2
	v_lshl_add_u32 v3, v36, 5, v3
	ds_write_b128 v3, v[4:7]
	ds_write_b128 v3, v[8:11] offset:16
